# NSA tile loop: deeper LDS prefetch for PV/QK + batched RMW; MoE gate-up unit order remapped so an XCD shares 4 weight tiles x 8 panels
# speedup vs baseline: 1.0047x; 1.0047x over previous
; #define LAS __attribute__((address_space(3)))
; __device__ __forceinline__ unsigned xb_add(unsigned* p, unsigned v) { return __hip_atomic_fetch_add(p, v, __ATOMIC_RELAXED, __HIP_MEMORY_SCOPE_AGENT); }
; __device__ __forceinline__ unsigned xb_xcc_id() { return (unsigned)__builtin_amdgcn_s_getreg((3 << 11) | 20) & 0xFu; }
; __device__ __forceinline__ XcdBarrier xcd_barrier_post(unsigned* bar, volatile LAS unsigned* st) {
;     XcdBarrier b; b.bar = bar; b.x = xb_xcc_id(); b.st = st;
;     if (threadIdx.x == 0) (void)xb_add(&bar[XB_XCNT(b.x)], 1u);
;     return b;
; __global__ void __launch_bounds__(512, 2) mk_fwd(Args a) {
;     extern __shared__ __attribute__((aligned(16))) unsigned char lds_raw[];
;     LAS unsigned char* lds = (LAS unsigned char*)lds_raw;
;     volatile LAS unsigned* MISC = (volatile LAS unsigned*)(lds + MISC_OFF);
;     if (threadIdx.x < 64) MISC[threadIdx.x] = 0u;
;     __syncthreads();
;     const int lo = a.ph_lo, hi = a.ph_hi;
;     ...
;     XcdBarrier bar = xcd_barrier_post((unsigned*)(a.ws + WS_CTL) + CW_BAR, MISC + 8);
_Z6mk_fwd4Args:
	s_load_dwordx8 s[60:67], s[0:1], 0xc0
	v_writelane_b32 v255, s2, 0
	s_load_dword s98, s[0:1], 0xf0
	s_and_b32 s99, s2, 7
	s_lshl_b32 s99, s99, 5
	s_lshr_b32 s100, s2, 3
	s_or_b32 s99, s99, s100
	s_waitcnt lgkmcnt(0)
	s_cmp_eq_u32 s98, 0x100
	s_cselect_b32 s99, s99, s2
	v_writelane_b32 v255, s99, 62
	v_writelane_b32 v255, s0, 1
	s_load_dwordx2 s[4:5], s[0:1], 0xe0
	v_cmp_gt_u32_e32 vcc, 64, v0
	v_writelane_b32 v255, s1, 2
	s_and_saveexec_b64 s[0:1], vcc
	v_lshl_add_u32 v1, v0, 2, 0
	v_add_u32_e32 v1, 0x24400, v1
	v_mov_b32_e32 v2, 0
	ds_write_b32 v1, v2
	s_waitcnt lgkmcnt(0)
	v_writelane_b32 v255, s4, 3
	s_nop 1
	v_writelane_b32 v255, s5, 4
	s_or_b64 exec, exec, s[0:1]
	s_add_u32 s0, s66, 0x4000
	s_addc_u32 s1, s67, 0
	v_writelane_b32 v255, s0, 5
	s_barrier
	s_nop 0
	v_writelane_b32 v255, s1, 6
	s_getreg_b32 s0, hwreg(HW_REG_XCC_ID, 0, 4)
	s_and_b32 s0, s0, 15
	v_writelane_b32 v255, s0, 7
	v_cmp_ne_u32_e64 s[0:1], 0, v0
	v_cmp_eq_u32_e64 s[2:3], 0, v0
	s_nop 0
	v_writelane_b32 v255, s0, 8
	s_nop 1
	v_writelane_b32 v255, s1, 9
	s_mov_b64 s[0:1], exec
	v_writelane_b32 v255, s2, 10
	s_nop 1
	v_writelane_b32 v255, s3, 11
	s_and_b64 s[2:3], s[0:1], s[2:3]
	s_mov_b64 exec, s[2:3]
	s_cbranch_execz .LBB0_5
	s_mov_b64 s[2:3], exec
	v_mbcnt_lo_u32_b32 v1, s2, 0
	v_mbcnt_hi_u32_b32 v1, s3, v1
	v_cmp_eq_u32_e32 vcc, 0, v1
	s_and_b64 s[4:5], exec, vcc
	s_mov_b64 exec, s[4:5]
	s_cbranch_execz .LBB0_5
	v_readlane_b32 s4, v255, 7
	s_bcnt1_i32_b64 s2, s[2:3]
	s_lshl_b32 s4, s4, 8
	v_mov_b32_e32 v2, s2
	v_readlane_b32 s2, v255, 5
	v_mov_b32_e32 v1, s4
	v_readlane_b32 s3, v255, 6
	s_nop 4
	global_atomic_add v1, v2, s[2:3] offset:1024

; #define PG8_STAGE(bufoff, gbase, voff) do { _Pragma("unroll") for (int _i = 0; _i < 2; ++_i) \
;         __builtin_amdgcn_global_load_lds((const unsigned*)((const char*)(gbase) + (voff)[_i]), (PG8_LAS unsigned*)(lds + (bufoff) + ldsw + _i * 8192), 16, 0, 0); } while (0)
; #define PG8_WAIT_V(n) asm volatile("s_waitcnt vmcnt(" #n ")" ::: "memory")
; #define PG8_BAR __builtin_amdgcn_s_barrier()
; template <class Epi, class Sched, bool ALIGN_EPI = false, bool SP2 = false, bool FP8 = false>
; __device__ __forceinline__ void gemm_phase(PG8_LAS unsigned char* lds, const Gemm g, const Sched& S, const Epi& E) {
;     ...
;     const char* cA = (const char*)g.A + (size_t)cur.pm * tstep; const char* cB = (const char*)g.Bt + (size_t)cur.pb * tstep;
;     S.a_ready(cur);
;     if constexpr (SP2) {
;         PG8_STAGE(PG8_SB(0, 0), cB, voffB); PG8_STAGE(PG8_SB(0, 1), cB + hstep, voffB); PG8_STAGE(PG8_SA(0, 0), cA, voffA); PG8_STAGE(PG8_SA(0, 1), cA + hstep, voffA);
;         if (wr == 1) PG8_BAR;
;         PG8_WAIT_V(2); PG8_BAR;
;         PG8_STAGE(PG8_SB(1, 0), cB + kstep, voffB); PG8_STAGE(PG8_SA(1, 0), cA + kstep, voffA); PG8_STAGE(PG8_SB(1, 1), cB + hstep + kstep, voffB);
;         PG8_WAIT_V(6); PG8_BAR;
;     __device__ __forceinline__ void init(const int* moe_base, int N, int G_, int c_) { nP = __builtin_amdgcn_readfirstlane(moe_base[8]) >> 8; nN = N / 256; nU = nP * nN; G = G_; c = c_;
;         b1 = __builtin_amdgcn_readfirstlane(moe_base[1]); b2 = __builtin_amdgcn_readfirstlane(moe_base[2]); b3 = __builtin_amdgcn_readfirstlane(moe_base[3]); b4 = __builtin_amdgcn_readfirstlane(moe_base[4]);
;         b5 = __builtin_amdgcn_readfirstlane(moe_base[5]); b6 = __builtin_amdgcn_readfirstlane(moe_base[6]); b7 = __builtin_amdgcn_readfirstlane(moe_base[7]); }
;     __device__ __forceinline__ bool next(int i, pg8::Unit& u) const {
;         const int L = i * G + c; if (L >= nU) return false;
;         const int nig = 8 * nN, gid = L / nig, fm = gid * 8, gsz = (nP - fm) < 8 ? (nP - fm) : 8, r = L % nig;
;         u.pm = fm + r % gsz; u.pn = r / gsz;
;         const int row0 = u.pm * 256; const int e = (row0 >= b1) + (row0 >= b2) + (row0 >= b3) + (row0 >= b4) + (row0 >= b5) + (row0 >= b6) + (row0 >= b7);
;         u.pb = e * nN + u.pn; return true;
.LBB0_2174:
	s_cmp_lt_i32 s78, 23
	s_cselect_b64 s[0:1], -1, 0
	s_and_b64 s[2:3], s[0:1], s[2:3]
	s_andn2_b64 vcc, exec, s[2:3]
	s_cbranch_vccnz .LBB0_2191
	s_add_u32 s2, s66, 0xa80004
	s_addc_u32 s3, s67, 0
	v_mov_b32_e32 v163, 0
	v_mov_b32_e32 v1, 0xa80000
	global_load_dwordx4 v[2:5], v163, s[2:3] offset:16
	global_load_dwordx4 v[6:9], v1, s[66:67] offset:4
	v_readfirstlane_b32 s8, v0
	s_waitcnt vmcnt(0)
	v_readfirstlane_b32 s2, v5
	s_ashr_i32 s36, s2, 8
	s_mul_i32 s37, s36, 56
	v_readlane_b32 s2, v255, 62
	v_readfirstlane_b32 s11, v6
	v_readfirstlane_b32 s30, v7
	v_readfirstlane_b32 s31, v8
	v_readfirstlane_b32 s33, v9
	v_readfirstlane_b32 s34, v2
	v_readfirstlane_b32 s35, v3
	v_readfirstlane_b32 s38, v4
	s_cmp_ge_i32 s2, s37
	s_cbranch_scc1 .LBB0_2191
	v_lshrrev_b32_e32 v1, 5, v0
	v_lshrrev_b32_e32 v3, 1, v0
	v_and_b32_e32 v1, 4, v1
	v_bfe_u32 v2, v0, 2, 2
	v_and_b32_e32 v13, 24, v3
	v_or3_b32 v1, v1, v2, v13
	v_lshlrev_b32_e32 v2, 4, v0
	v_or_b32_e32 v10, 0x2000, v2
	s_add_u32 s39, s66, 0x28800000
	v_lshrrev_b32_e32 v3, 7, v10
	s_movk_i32 s2, 0x60
	s_addc_u32 s40, s67, 0
	v_and_or_b32 v4, v3, s2, v1
	v_bfe_u32 v14, v0, 2, 4
	s_movk_i32 s2, 0x70
	v_readlane_b32 s7, v255, 62
	s_add_u32 s41, s66, 0x4a000000
	v_and_or_b32 v3, v3, s2, v14
	s_mul_hi_i32 s2, s7, 0x92492493
	s_waitcnt lgkmcnt(0)
	s_addc_u32 s42, s67, 0
	s_add_i32 s2, s2, s7
	s_lshr_b32 s3, s2, 31
	s_ashr_i32 s2, s2, 8
	s_add_i32 s2, s2, s3
	s_lshl_b32 s3, s2, 3
	v_and_b32_e32 v5, 32, v0
	s_sub_i32 s4, s36, s3
	v_bitop3_b32 v11, v2, v5, 48 bitop3:0x6c
	v_and_b32_e32 v12, 64, v0
	s_min_i32 s4, s4, 8
	v_or_b32_e32 v2, v11, v12
	s_abs_i32 s5, s4
	v_lshl_or_b32 v164, v4, 11, v2
	v_cvt_f32_u32_e32 v4, s5
	v_lshl_or_b32 v166, v3, 11, v2
	v_lshrrev_b32_e32 v3, 3, v0
	v_and_or_b32 v1, v3, 32, v1
	v_lshl_or_b32 v162, v1, 11, v2
	v_and_or_b32 v1, v3, 48, v14
	v_lshl_or_b32 v168, v1, 11, v2
	v_rcp_iflag_f32_e32 v1, v4
	s_sub_i32 s12, 0, s5
	s_mulk_i32 s2, 0x1c0
	s_sub_i32 s2, s7, s2
	v_mul_f32_e32 v1, 0x4f7ffffe, v1
	v_cvt_u32_f32_e32 v1, v1
	s_abs_i32 s10, s2
	s_lshr_b32 s6, s8, 6
	s_xor_b32 s7, s2, s4
	v_readfirstlane_b32 s13, v1
	s_mul_i32 s12, s12, s13
	s_mul_hi_u32 s12, s13, s12
	s_add_i32 s13, s13, s12
	s_mul_hi_u32 s12, s10, s13
	s_mul_i32 s13, s12, s5
	s_sub_i32 s10, s10, s13
	s_lshr_b32 s9, s8, 8
	s_lshl_b32 s43, s6, 10
	s_ashr_i32 s7, s7, 31
	s_add_i32 s13, s12, 1
	s_sub_i32 s14, s10, s5
	s_cmp_ge_u32 s10, s5
	s_cselect_b32 s12, s13, s12
	s_cselect_b32 s10, s14, s10
	s_add_i32 s13, s12, 1
	s_cmp_ge_u32 s10, s5
	s_cselect_b32 s5, s13, s12
	s_xor_b32 s5, s5, s7
	s_sub_i32 s55, s5, s7
	s_mul_i32 s4, s55, s4
	s_sub_i32 s2, s2, s4
	s_add_i32 s22, s2, s3
	s_lshl_b32 s4, s22, 8
	s_cmp_ge_i32 s4, s11
	s_cselect_b64 s[2:3], -1, 0
	s_cmp_ge_i32 s4, s30
	v_cndmask_b32_e64 v1, 0, 1, s[2:3]
	s_cselect_b64 s[2:3], -1, 0
	s_cmp_ge_i32 s4, s31
	v_cndmask_b32_e64 v2, 0, 1, s[2:3]
	s_cselect_b64 s[2:3], -1, 0
	v_readfirstlane_b32 s5, v2
	v_readfirstlane_b32 s7, v1
	s_cmp_lg_u64 s[2:3], 0
	s_addc_u32 s5, s5, s7
	s_cmp_ge_i32 s4, s33
	s_cselect_b64 s[2:3], -1, 0
	s_cmp_ge_i32 s4, s34
	v_cndmask_b32_e64 v1, 0, 1, s[2:3]
	s_cselect_b64 s[2:3], -1, 0
	v_readfirstlane_b32 s7, v1
	s_cmp_lg_u64 s[2:3], 0
	s_addc_u32 s5, s5, s7
	s_cmp_ge_i32 s4, s35
	s_cselect_b64 s[2:3], -1, 0
	s_cmp_ge_i32 s4, s38
	v_cndmask_b32_e64 v1, 0, 1, s[2:3]
	s_cselect_b64 s[2:3], -1, 0
	v_readfirstlane_b32 s4, v1
	s_cmp_lg_u64 s[2:3], 0
	s_addc_u32 s2, s5, s4
	s_mul_i32 s2, s2, 56
	s_add_i32 s2, s2, s55
	s_ashr_i32 s3, s2, 31
	s_ashr_i32 s23, s22, 31
	s_lshl_b64 s[2:3], s[2:3], 19
	s_lshl_b64 s[4:5], s[22:23], 19
	s_add_u32 s26, s41, s2
	s_addc_u32 s27, s42, s3
	s_add_i32 s23, s43, 0
	s_add_i32 m0, s23, 0x10000
	v_mov_b32_e32 v165, v163
	global_load_lds_dwordx4 v162, s[26:27]
	s_add_i32 m0, s23, 0x12000
	s_add_u32 s2, s26, 0x40000
	global_load_lds_dwordx4 v164, s[26:27]
	s_addc_u32 s3, s27, 0
	s_add_i32 m0, s23, 0x14000
	v_mov_b32_e32 v169, v163
	global_load_lds_dwordx4 v162, s[2:3]
	s_add_i32 m0, s23, 0x16000
	s_add_u32 s24, s39, s4
	s_addc_u32 s25, s40, s5
	s_add_i32 s44, s23, 0x2000
	global_load_lds_dwordx4 v164, s[2:3]
	s_mov_b32 m0, s23
	s_add_u32 s2, s24, 0x40000
	global_load_lds_dwordx4 v168, s[24:25]
	s_mov_b32 m0, s44
	s_addc_u32 s3, s25, 0
	s_add_i32 s45, s23, 0x4000
	global_load_lds_dwordx4 v166, s[24:25]
	s_mov_b32 m0, s45
	s_add_i32 s46, s23, 0x6000
	global_load_lds_dwordx4 v168, s[2:3]
	s_mov_b32 m0, s46
	v_mov_b32_e32 v167, v163
	global_load_lds_dwordx4 v166, s[2:3]
	v_readlane_b32 s2, v255, 1
	v_readlane_b32 s3, v255, 2
	s_load_dword s47, s[2:3], 0xf0
	s_cmp_eq_u32 s9, 1
	s_mov_b32 s48, 0
	v_lshl_add_u64 v[8:9], s[26:27], 0, v[162:163]
	v_lshl_add_u64 v[6:7], s[26:27], 0, v[164:165]
	v_lshl_add_u64 v[2:3], s[24:25], 0, v[168:169]
	s_cselect_b64 s[2:3], -1, 0
	s_cmp_lg_u32 s9, 1
	v_lshl_add_u64 v[4:5], s[24:25], 0, v[166:167]
	s_cbranch_scc1 .LBB0_2178
	s_barrier

; template <class Epi, class Sched, bool ALIGN_EPI = false, bool SP2 = false, bool FP8 = false>
; __device__ __forceinline__ void gemm_phase(PG8_LAS unsigned char* lds, const Gemm g, const Sched& S, const Epi& E) {
;     ...
;         const bool has_next = S.next(ui + 1, nxt);
;         const char* nA = has_next ? (const char*)g.A + (size_t)nxt.pm * tstep : cA; const char* nB = has_next ? (const char*)g.Bt + (size_t)nxt.pb * tstep : cB;
;     __device__ __forceinline__ bool next(int i, pg8::Unit& u) const {
;         const int L = i * G + c; if (L >= nU) return false;
;         const int nig = 8 * nN, gid = L / nig, fm = gid * 8, gsz = (nP - fm) < 8 ? (nP - fm) : 8, r = L % nig;
;         u.pm = fm + r % gsz; u.pn = r / gsz;
;         const int row0 = u.pm * 256; const int e = (row0 >= b1) + (row0 >= b2) + (row0 >= b3) + (row0 >= b4) + (row0 >= b5) + (row0 >= b6) + (row0 >= b7);
;         u.pb = e * nN + u.pn; return true;
.LBB0_2181:
	s_add_i32 s48, s48, 1
	s_waitcnt lgkmcnt(0)
	s_mul_i32 s13, s48, s47
	v_readlane_b32 s14, v255, 62
	s_add_i32 s13, s13, s14
	s_cmp_lt_i32 s13, s37
	s_cselect_b64 s[14:15], -1, 0
	s_cmp_ge_i32 s13, s37
	s_cbranch_scc1 .LBB0_2183
	s_mul_hi_i32 s12, s13, 0x92492493
	s_add_i32 s12, s12, s13
	s_lshr_b32 s16, s12, 31
	s_ashr_i32 s12, s12, 8
	s_add_i32 s12, s12, s16
	s_lshl_b32 s16, s12, 3
	s_sub_i32 s17, s36, s16
	s_min_i32 s17, s17, 8
	s_abs_i32 s18, s17
	v_cvt_f32_u32_e32 v2, s18
	s_sub_i32 s20, 0, s18
	s_mulk_i32 s12, 0x1c0
	s_sub_i32 s12, s13, s12
	v_rcp_iflag_f32_e32 v2, v2
	s_abs_i32 s13, s12
	s_xor_b32 s19, s12, s17
	s_ashr_i32 s19, s19, 31
	v_mul_f32_e32 v2, 0x4f7ffffe, v2
	v_cvt_u32_f32_e32 v2, v2
	s_nop 0
	v_readfirstlane_b32 s21, v2
	s_mul_i32 s20, s20, s21
	s_mul_hi_u32 s20, s21, s20
	s_add_i32 s21, s21, s20
	s_mul_hi_u32 s20, s13, s21
	s_mul_i32 s21, s20, s18
	s_sub_i32 s13, s13, s21
	s_add_i32 s28, s20, 1
	s_sub_i32 s21, s13, s18
	s_cmp_ge_u32 s13, s18
	s_cselect_b32 s20, s28, s20
	s_cselect_b32 s13, s21, s13
	s_add_i32 s21, s20, 1
	s_cmp_ge_u32 s13, s18
	s_cselect_b32 s13, s21, s20
	s_xor_b32 s13, s13, s19
	s_sub_i32 s54, s13, s19
	s_mul_i32 s13, s54, s17
	s_sub_i32 s12, s12, s13
	s_add_i32 s12, s12, s16
	s_lshl_b32 s13, s12, 8
	s_cmp_ge_i32 s13, s11
	s_cselect_b64 s[16:17], -1, 0
	s_cmp_ge_i32 s13, s30
	v_cndmask_b32_e64 v2, 0, 1, s[16:17]
	s_cselect_b64 s[16:17], -1, 0
	s_cmp_ge_i32 s13, s31
	v_cndmask_b32_e64 v3, 0, 1, s[16:17]
	s_cselect_b64 s[16:17], -1, 0
	v_readfirstlane_b32 s18, v3
	v_readfirstlane_b32 s19, v2
	s_cmp_lg_u64 s[16:17], 0
	s_addc_u32 s18, s18, s19
	s_cmp_ge_i32 s13, s33
	s_cselect_b64 s[16:17], -1, 0
	s_cmp_ge_i32 s13, s34
	v_cndmask_b32_e64 v2, 0, 1, s[16:17]
	s_cselect_b64 s[16:17], -1, 0
	v_readfirstlane_b32 s19, v2
	s_cmp_lg_u64 s[16:17], 0
	s_addc_u32 s18, s18, s19
	s_cmp_ge_i32 s13, s35
	s_cselect_b64 s[16:17], -1, 0
	s_cmp_ge_i32 s13, s38
	v_cndmask_b32_e64 v2, 0, 1, s[16:17]
	s_cselect_b64 s[16:17], -1, 0
	v_readfirstlane_b32 s13, v2
	s_cmp_lg_u64 s[16:17], 0
	s_addc_u32 s13, s18, s13
	s_mul_i32 s13, s13, 56
	s_add_i32 s16, s13, s54

; __global__ void __launch_bounds__(512, 2) mk_fwd(Args a) {
	.amdhsa_kernel _Z6mk_fwd4Args
		.amdhsa_group_segment_fixed_size 0
		.amdhsa_private_segment_fixed_size 0
		.amdhsa_kernarg_size 496
		.amdhsa_user_sgpr_count 2
		.amdhsa_user_sgpr_dispatch_ptr 0
		.amdhsa_user_sgpr_queue_ptr 0
		.amdhsa_user_sgpr_kernarg_segment_ptr 1
		.amdhsa_user_sgpr_dispatch_id 0
		.amdhsa_user_sgpr_kernarg_preload_length 0
		.amdhsa_user_sgpr_kernarg_preload_offset 0
		.amdhsa_user_sgpr_private_segment_size 0
		.amdhsa_uses_dynamic_stack 0
		.amdhsa_enable_private_segment 0
		.amdhsa_system_sgpr_workgroup_id_x 1
		.amdhsa_system_sgpr_workgroup_id_y 0
		.amdhsa_system_sgpr_workgroup_id_z 0
		.amdhsa_system_sgpr_workgroup_info 0
		.amdhsa_system_vgpr_workitem_id 0
		.amdhsa_next_free_vgpr 256
		.amdhsa_next_free_sgpr 102
		.amdhsa_accum_offset 256
		.amdhsa_reserve_vcc 1
		.amdhsa_float_round_mode_32 0
		.amdhsa_float_round_mode_16_64 0
		.amdhsa_float_denorm_mode_32 3
		.amdhsa_float_denorm_mode_16_64 3
		.amdhsa_dx10_clamp 1
		.amdhsa_ieee_mode 1
		.amdhsa_fp16_overflow 0
		.amdhsa_tg_split 0
		.amdhsa_exception_fp_ieee_invalid_op 0
		.amdhsa_exception_fp_denorm_src 0
		.amdhsa_exception_fp_ieee_div_zero 0
		.amdhsa_exception_fp_ieee_overflow 0
		.amdhsa_exception_fp_ieee_underflow 0
		.amdhsa_exception_fp_ieee_inexact 0
		.amdhsa_exception_int_div_zero 0
	.end_amdhsa_kernel

; __global__ void __launch_bounds__(512, 2) mk_fwd(Args a) {
amdhsa.kernels:
  - .agpr_count:     0
    .args:
      - .offset:         0
        .size:           240
        .value_kind:     by_value
      - .offset:         240
        .size:           4
        .value_kind:     hidden_block_count_x
      - .offset:         244
        .size:           4
        .value_kind:     hidden_block_count_y
      - .offset:         248
        .size:           4
        .value_kind:     hidden_block_count_z
      - .offset:         252
        .size:           2
        .value_kind:     hidden_group_size_x
      - .offset:         254
        .size:           2
        .value_kind:     hidden_group_size_y
      - .offset:         256
        .size:           2
        .value_kind:     hidden_group_size_z
      - .offset:         258
        .size:           2
        .value_kind:     hidden_remainder_x
      - .offset:         260
        .size:           2
        .value_kind:     hidden_remainder_y
      - .offset:         262
        .size:           2
        .value_kind:     hidden_remainder_z
      - .offset:         280
        .size:           8
        .value_kind:     hidden_global_offset_x
      - .offset:         288
        .size:           8
        .value_kind:     hidden_global_offset_y
      - .offset:         296
        .size:           8
        .value_kind:     hidden_global_offset_z
      - .offset:         304
        .size:           2
        .value_kind:     hidden_grid_dims
      - .offset:         360
        .size:           4
        .value_kind:     hidden_dynamic_lds_size
    .group_segment_fixed_size: 0
    .kernarg_segment_align: 8
    .kernarg_segment_size: 496
    .language:       OpenCL C
    .language_version:
      - 2
      - 0
    .max_flat_workgroup_size: 512
    .name:           _Z6mk_fwd4Args
    .private_segment_fixed_size: 0
    .sgpr_count:     108
    .sgpr_spill_count: 76
    .symbol:         _Z6mk_fwd4Args.kd
    .uniform_work_group_size: 1
    .uses_dynamic_stack: false
    .vgpr_count:     256
    .vgpr_spill_count: 0
    .wavefront_size: 64
